# baseline (speedup 1.0000x reference)
.LBB1_4:
	v_add_u32_e32 v182, s19, v191
	v_add_u32_e32 v238, s19, v192
	ds_read_b128 v[178:181], v182 offset:32768
	ds_read_b128 v[194:197], v182 offset:34816
	ds_read_b128 v[198:201], v182 offset:36864
	ds_read_b128 v[202:205], v182 offset:38912
	ds_read_b128 v[206:209], v238
	ds_read_b128 v[210:213], v238 offset:2048
	ds_read_b128 v[214:217], v238 offset:4096
	ds_read_b128 v[218:221], v238 offset:6144
	ds_read_b128 v[222:225], v238 offset:8192
	ds_read_b128 v[226:229], v238 offset:10240
	ds_read_b128 v[230:233], v238 offset:12288
	ds_read_b128 v[234:237], v238 offset:14336
	s_min_u32 s21, s20, 29
	s_xor_b32 s19, s19, 0x10000
	v_add_u32_e32 v239, s19, v189
	s_waitcnt vmcnt(11)
	v_cvt_pk_bf16_f32 v13, v12, v13
	v_cvt_pk_bf16_f32 v12, v10, v11
	s_waitcnt vmcnt(10)
	v_cvt_pk_bf16_f32 v11, v20, v21
	v_cvt_pk_bf16_f32 v10, v18, v19
	ds_write2st64_b64 v239, v[12:13], v[10:11] offset1:8
	s_waitcnt vmcnt(9)
	v_cvt_pk_bf16_f32 v11, v24, v25
	v_cvt_pk_bf16_f32 v10, v22, v23
	s_waitcnt vmcnt(8)
	v_cvt_pk_bf16_f32 v13, v32, v33
	v_cvt_pk_bf16_f32 v12, v30, v31
	ds_write2st64_b64 v239, v[10:11], v[12:13] offset0:16 offset1:24
	s_waitcnt vmcnt(7)
	v_cvt_pk_bf16_f32 v11, v36, v37
	v_cvt_pk_bf16_f32 v10, v34, v35
	s_waitcnt vmcnt(6)
	v_cvt_pk_bf16_f32 v13, v40, v41
	v_cvt_pk_bf16_f32 v12, v38, v39
	ds_write2st64_b64 v239, v[10:11], v[12:13] offset0:32 offset1:40
	s_waitcnt vmcnt(5)
	v_cvt_pk_bf16_f32 v11, v44, v45
	v_cvt_pk_bf16_f32 v10, v42, v43
	s_waitcnt vmcnt(4)
	v_cvt_pk_bf16_f32 v13, v48, v49
	v_cvt_pk_bf16_f32 v12, v46, v47
	ds_write2st64_b64 v239, v[10:11], v[12:13] offset0:48 offset1:56
	s_waitcnt lgkmcnt(0)
	s_add_i32 s21, s21, 2
	s_barrier
	s_setprio 1
	s_lshl_b32 s22, s21, 1
	s_and_b32 s22, s22, 0x60
	s_add_i32 s22, s22, s12
	s_lshl_b32 s22, s22, 6
	s_and_b32 s22, s22, 0x3f00
	s_or_b32 s22, s22, s13
	s_lshl_b32 s23, s21, 23
	s_lshl_b32 s22, s22, 9
	s_and_b32 s23, s23, 0x7000000
	s_or_b32 s22, s22, s23
	s_lshl_b32 s23, s21, 8
	s_and_b32 s23, s23, 0x100
	s_or_b32 s22, s22, s23
	s_or_b32 s23, s22, 0x4000
	s_waitcnt lgkmcnt(11)
	buffer_load_dwordx4 v[10:13], v1, s[4:7], s22 offen sc0 nt
	buffer_load_dwordx4 v[18:21], v1, s[4:7], s23 offen sc0 nt
	s_or_b32 s23, s22, 0x8000
	buffer_load_dwordx4 v[22:25], v1, s[4:7], s23 offen sc0 nt
	s_or_b32 s23, s22, 0xc000
	buffer_load_dwordx4 v[30:33], v1, s[4:7], s23 offen sc0 nt
	s_or_b32 s23, s22, 0x10000
	buffer_load_dwordx4 v[34:37], v1, s[4:7], s23 offen sc0 nt
	s_or_b32 s23, s22, 0x14000
	buffer_load_dwordx4 v[38:41], v1, s[4:7], s23 offen sc0 nt
	s_or_b32 s23, s22, 0x18000
	s_or_b32 s22, s22, 0x1c000
	buffer_load_dwordx4 v[42:45], v1, s[4:7], s23 offen sc0 nt
	buffer_load_dwordx4 v[46:49], v1, s[4:7], s22 offen sc0 nt
	v_mfma_f32_16x16x32_bf16 v[174:177], v[178:181], v[206:209], v[174:177]
	v_mfma_f32_16x16x32_bf16 v[170:173], v[194:197], v[206:209], v[170:173]
	v_mfma_f32_16x16x32_bf16 v[158:161], v[198:201], v[206:209], v[158:161]
	v_mfma_f32_16x16x32_bf16 v[142:145], v[202:205], v[206:209], v[142:145]
	s_waitcnt lgkmcnt(10)
	v_mfma_f32_16x16x32_bf16 v[166:169], v[178:181], v[210:213], v[166:169]
	v_mfma_f32_16x16x32_bf16 v[162:165], v[194:197], v[210:213], v[162:165]
	v_mfma_f32_16x16x32_bf16 v[146:149], v[198:201], v[210:213], v[146:149]
	v_mfma_f32_16x16x32_bf16 v[122:125], v[202:205], v[210:213], v[122:125]
	s_waitcnt lgkmcnt(9)
	v_mfma_f32_16x16x32_bf16 v[154:157], v[178:181], v[214:217], v[154:157]
	v_mfma_f32_16x16x32_bf16 v[150:153], v[194:197], v[214:217], v[150:153]
	v_mfma_f32_16x16x32_bf16 v[130:133], v[198:201], v[214:217], v[130:133]
	v_mfma_f32_16x16x32_bf16 v[106:109], v[202:205], v[214:217], v[106:109]
	s_waitcnt lgkmcnt(8)
	v_mfma_f32_16x16x32_bf16 v[138:141], v[178:181], v[218:221], v[138:141]
	v_mfma_f32_16x16x32_bf16 v[134:137], v[194:197], v[218:221], v[134:137]
	v_mfma_f32_16x16x32_bf16 v[114:117], v[198:201], v[218:221], v[114:117]
	v_mfma_f32_16x16x32_bf16 v[90:93], v[202:205], v[218:221], v[90:93]
	s_waitcnt lgkmcnt(7)
	v_mfma_f32_16x16x32_bf16 v[126:129], v[178:181], v[222:225], v[126:129]
	v_mfma_f32_16x16x32_bf16 v[118:121], v[194:197], v[222:225], v[118:121]
	v_mfma_f32_16x16x32_bf16 v[98:101], v[198:201], v[222:225], v[98:101]
	v_mfma_f32_16x16x32_bf16 v[74:77], v[202:205], v[222:225], v[74:77]
	s_waitcnt lgkmcnt(6)
	v_mfma_f32_16x16x32_bf16 v[110:113], v[178:181], v[226:229], v[110:113]
	v_mfma_f32_16x16x32_bf16 v[102:105], v[194:197], v[226:229], v[102:105]
	v_mfma_f32_16x16x32_bf16 v[82:85], v[198:201], v[226:229], v[82:85]
	v_mfma_f32_16x16x32_bf16 v[62:65], v[202:205], v[226:229], v[62:65]
	s_waitcnt lgkmcnt(5)
	v_mfma_f32_16x16x32_bf16 v[94:97], v[178:181], v[230:233], v[94:97]
	v_mfma_f32_16x16x32_bf16 v[86:89], v[194:197], v[230:233], v[86:89]
	v_mfma_f32_16x16x32_bf16 v[70:73], v[198:201], v[230:233], v[70:73]
	v_mfma_f32_16x16x32_bf16 v[54:57], v[202:205], v[230:233], v[54:57]
	s_waitcnt lgkmcnt(4)
	v_mfma_f32_16x16x32_bf16 v[78:81], v[178:181], v[234:237], v[78:81]
	v_mfma_f32_16x16x32_bf16 v[66:69], v[194:197], v[234:237], v[66:69]
	v_mfma_f32_16x16x32_bf16 v[58:61], v[198:201], v[234:237], v[58:61]
	v_mfma_f32_16x16x32_bf16 v[50:53], v[202:205], v[234:237], v[50:53]
	s_setprio 0
	s_waitcnt lgkmcnt(0)
	s_barrier
	ds_read_b128 v[178:181], v182 offset:33792
	ds_read_b128 v[194:197], v182 offset:35840
	ds_read_b128 v[198:201], v182 offset:37888
	ds_read_b128 v[202:205], v182 offset:39936
	ds_read_b128 v[206:209], v238 offset:1024
	ds_read_b128 v[210:213], v238 offset:3072
	ds_read_b128 v[214:217], v238 offset:5120
	ds_read_b128 v[218:221], v238 offset:7168
	ds_read_b128 v[222:225], v238 offset:9216
	ds_read_b128 v[226:229], v238 offset:11264
	ds_read_b128 v[230:233], v238 offset:13312
	ds_read_b128 v[234:237], v238 offset:15360
	v_add_u32_e32 v182, s19, v190
	s_waitcnt vmcnt(11)
	ds_write_b128 v182, v[2:5] offset:32768
	s_waitcnt vmcnt(10)
	ds_write_b128 v182, v[6:9] offset:40960
	s_waitcnt vmcnt(9)
	ds_write_b128 v182, v[14:17] offset:49152
	s_waitcnt vmcnt(8)
	ds_write_b128 v182, v[26:29] offset:57344
	s_waitcnt lgkmcnt(0)
	s_barrier
	s_setprio 1
	s_lshl_b32 s21, s21, 7
	s_and_b32 s21, s21, 0x780
	s_or_b32 s21, s21, s14
	s_or_b32 s22, s21, 0x20000
	s_waitcnt lgkmcnt(11)
	v_mfma_f32_16x16x32_bf16 v[174:177], v[178:181], v[206:209], v[174:177]
	v_mfma_f32_16x16x32_bf16 v[170:173], v[194:197], v[206:209], v[170:173]
	v_mfma_f32_16x16x32_bf16 v[158:161], v[198:201], v[206:209], v[158:161]
	v_mfma_f32_16x16x32_bf16 v[142:145], v[202:205], v[206:209], v[142:145]
	s_waitcnt lgkmcnt(10)
	v_mfma_f32_16x16x32_bf16 v[166:169], v[178:181], v[210:213], v[166:169]
	v_mfma_f32_16x16x32_bf16 v[162:165], v[194:197], v[210:213], v[162:165]
	buffer_load_dwordx4 v[2:5], v188, s[0:3], s21 offen sc1
	v_mfma_f32_16x16x32_bf16 v[146:149], v[198:201], v[210:213], v[146:149]
	v_mfma_f32_16x16x32_bf16 v[122:125], v[202:205], v[210:213], v[122:125]
	s_waitcnt lgkmcnt(9)
	v_mfma_f32_16x16x32_bf16 v[154:157], v[178:181], v[214:217], v[154:157]
	v_mfma_f32_16x16x32_bf16 v[150:153], v[194:197], v[214:217], v[150:153]
	v_mfma_f32_16x16x32_bf16 v[130:133], v[198:201], v[214:217], v[130:133]
	v_mfma_f32_16x16x32_bf16 v[106:109], v[202:205], v[214:217], v[106:109]
	s_waitcnt lgkmcnt(8)
	v_mfma_f32_16x16x32_bf16 v[138:141], v[178:181], v[218:221], v[138:141]
	v_mfma_f32_16x16x32_bf16 v[134:137], v[194:197], v[218:221], v[134:137]
	buffer_load_dwordx4 v[6:9], v188, s[0:3], s22 offen sc1
	s_or_b32 s22, s21, 0x40000
	s_or_b32 s21, s21, 0x60000
	v_mfma_f32_16x16x32_bf16 v[114:117], v[198:201], v[218:221], v[114:117]
	v_mfma_f32_16x16x32_bf16 v[90:93], v[202:205], v[218:221], v[90:93]
	s_waitcnt lgkmcnt(7)
	v_mfma_f32_16x16x32_bf16 v[126:129], v[178:181], v[222:225], v[126:129]
	v_mfma_f32_16x16x32_bf16 v[118:121], v[194:197], v[222:225], v[118:121]
	v_mfma_f32_16x16x32_bf16 v[98:101], v[198:201], v[222:225], v[98:101]
	v_mfma_f32_16x16x32_bf16 v[74:77], v[202:205], v[222:225], v[74:77]
	s_waitcnt lgkmcnt(6)
	v_mfma_f32_16x16x32_bf16 v[110:113], v[178:181], v[226:229], v[110:113]
	v_mfma_f32_16x16x32_bf16 v[102:105], v[194:197], v[226:229], v[102:105]
	buffer_load_dwordx4 v[14:17], v188, s[0:3], s22 offen sc1
	v_mfma_f32_16x16x32_bf16 v[82:85], v[198:201], v[226:229], v[82:85]
	v_mfma_f32_16x16x32_bf16 v[62:65], v[202:205], v[226:229], v[62:65]
	s_waitcnt lgkmcnt(5)
	v_mfma_f32_16x16x32_bf16 v[94:97], v[178:181], v[230:233], v[94:97]
	v_mfma_f32_16x16x32_bf16 v[86:89], v[194:197], v[230:233], v[86:89]
	v_mfma_f32_16x16x32_bf16 v[70:73], v[198:201], v[230:233], v[70:73]
	v_mfma_f32_16x16x32_bf16 v[54:57], v[202:205], v[230:233], v[54:57]
	s_waitcnt lgkmcnt(4)
	v_mfma_f32_16x16x32_bf16 v[78:81], v[178:181], v[234:237], v[78:81]
	v_mfma_f32_16x16x32_bf16 v[66:69], v[194:197], v[234:237], v[66:69]
	buffer_load_dwordx4 v[26:29], v188, s[0:3], s21 offen sc1
	v_mfma_f32_16x16x32_bf16 v[58:61], v[198:201], v[234:237], v[58:61]
	v_mfma_f32_16x16x32_bf16 v[50:53], v[202:205], v[234:237], v[50:53]
	s_setprio 0
	s_and_b32 s21, s20, 15
	s_cmp_lg_u32 s21, 15
	s_cbranch_scc1 .LBB1_3
	s_and_b32 s21, s18, 32
	s_add_i32 s21, s21, s12
	s_lshl_b32 s21, s21, 6
	s_and_b32 s21, s21, 0x3f00
	v_add_lshl_u32 v182, v193, s21, 9
	v_lshl_add_u64 v[206:207], v[184:185], 0, v[182:183]
	v_add_co_u32_e32 v208, vcc, s8, v206
	s_nop 1
	v_addc_co_u32_e32 v209, vcc, 0, v207, vcc
	v_add_co_u32_e32 v210, vcc, s15, v206
	s_nop 1
	v_addc_co_u32_e32 v211, vcc, 0, v207, vcc
	v_add_co_u32_e32 v212, vcc, s9, v206
	s_nop 1
	v_addc_co_u32_e32 v213, vcc, 0, v207, vcc
	v_add_co_u32_e32 v214, vcc, s16, v206
	s_nop 1
	v_addc_co_u32_e32 v215, vcc, 0, v207, vcc
	v_add_co_u32_e32 v216, vcc, s10, v206
	s_nop 1
	v_addc_co_u32_e32 v217, vcc, 0, v207, vcc
	v_add_co_u32_e32 v218, vcc, s17, v206
	s_nop 1
	v_addc_co_u32_e32 v219, vcc, 0, v207, vcc
	v_add_co_u32_e32 v220, vcc, s11, v206
	s_nop 1
	v_addc_co_u32_e32 v221, vcc, 0, v207, vcc
	global_store_dwordx4 v[206:207], v[174:177], off
	global_store_dwordx4 v[206:207], v[170:173], off offset:64
	global_store_dwordx4 v[206:207], v[158:161], off offset:128
	global_store_dwordx4 v[206:207], v[142:145], off offset:192
	global_store_dwordx4 v[208:209], v[166:169], off
	global_store_dwordx4 v[208:209], v[162:165], off offset:64
	global_store_dwordx4 v[208:209], v[146:149], off offset:128
	global_store_dwordx4 v[208:209], v[122:125], off offset:192
	global_store_dwordx4 v[210:211], v[154:157], off
	global_store_dwordx4 v[210:211], v[150:153], off offset:64
	global_store_dwordx4 v[210:211], v[130:133], off offset:128
	global_store_dwordx4 v[210:211], v[106:109], off offset:192
	global_store_dwordx4 v[212:213], v[138:141], off
	global_store_dwordx4 v[212:213], v[134:137], off offset:64
	global_store_dwordx4 v[212:213], v[114:117], off offset:128
	global_store_dwordx4 v[212:213], v[90:93], off offset:192
	global_store_dwordx4 v[214:215], v[126:129], off
	global_store_dwordx4 v[214:215], v[118:121], off offset:64
	global_store_dwordx4 v[214:215], v[98:101], off offset:128
	global_store_dwordx4 v[214:215], v[74:77], off offset:192
	global_store_dwordx4 v[216:217], v[110:113], off
	global_store_dwordx4 v[216:217], v[102:105], off offset:64
	global_store_dwordx4 v[216:217], v[82:85], off offset:128
	global_store_dwordx4 v[216:217], v[62:65], off offset:192
	global_store_dwordx4 v[218:219], v[94:97], off
	global_store_dwordx4 v[218:219], v[86:89], off offset:64
	global_store_dwordx4 v[218:219], v[70:73], off offset:128
	global_store_dwordx4 v[218:219], v[54:57], off offset:192
	global_store_dwordx4 v[220:221], v[78:81], off
	global_store_dwordx4 v[220:221], v[66:69], off offset:64
	global_store_dwordx4 v[220:221], v[58:61], off offset:128
	global_store_dwordx4 v[220:221], v[50:53], off offset:192
.Lpd_tail:
	s_waitcnt lgkmcnt(0)
	s_barrier
	s_add_i32 s20, s20, 1
	s_add_i32 s18, s18, 2
	v_add_u32_e32 v182, s19, v191
	v_add_u32_e32 v238, s19, v192
	ds_read_b128 v[178:181], v182 offset:32768
	ds_read_b128 v[194:197], v182 offset:34816
	ds_read_b128 v[198:201], v182 offset:36864
	ds_read_b128 v[202:205], v182 offset:38912
	ds_read_b128 v[206:209], v238
	ds_read_b128 v[210:213], v238 offset:2048
	ds_read_b128 v[214:217], v238 offset:4096
	ds_read_b128 v[218:221], v238 offset:6144
	ds_read_b128 v[222:225], v238 offset:8192
	ds_read_b128 v[226:229], v238 offset:10240
	ds_read_b128 v[230:233], v238 offset:12288
	ds_read_b128 v[234:237], v238 offset:14336
	s_min_u32 s21, s20, 29
	s_xor_b32 s19, s19, 0x10000
	v_add_u32_e32 v239, s19, v189
	s_waitcnt vmcnt(43)
	v_cvt_pk_bf16_f32 v13, v12, v13
	v_cvt_pk_bf16_f32 v12, v10, v11
	s_waitcnt vmcnt(42)
	v_cvt_pk_bf16_f32 v11, v20, v21
	v_cvt_pk_bf16_f32 v10, v18, v19
	ds_write2st64_b64 v239, v[12:13], v[10:11] offset1:8
	s_waitcnt vmcnt(41)
	v_cvt_pk_bf16_f32 v11, v24, v25
	v_cvt_pk_bf16_f32 v10, v22, v23
	s_waitcnt vmcnt(40)
	v_cvt_pk_bf16_f32 v13, v32, v33
	v_cvt_pk_bf16_f32 v12, v30, v31
	ds_write2st64_b64 v239, v[10:11], v[12:13] offset0:16 offset1:24
	s_waitcnt vmcnt(39)
	v_cvt_pk_bf16_f32 v11, v36, v37
	v_cvt_pk_bf16_f32 v10, v34, v35
	s_waitcnt vmcnt(38)
	v_cvt_pk_bf16_f32 v13, v40, v41
	v_cvt_pk_bf16_f32 v12, v38, v39
	ds_write2st64_b64 v239, v[10:11], v[12:13] offset0:32 offset1:40
	s_waitcnt vmcnt(37)
	v_cvt_pk_bf16_f32 v11, v44, v45
	v_cvt_pk_bf16_f32 v10, v42, v43
	s_waitcnt vmcnt(36)
	v_cvt_pk_bf16_f32 v13, v48, v49
	v_cvt_pk_bf16_f32 v12, v46, v47
	ds_write2st64_b64 v239, v[10:11], v[12:13] offset0:48 offset1:56
	s_waitcnt lgkmcnt(0)
	s_add_i32 s21, s21, 2
	s_barrier
	s_setprio 1
	s_lshl_b32 s22, s21, 1
	s_and_b32 s22, s22, 0x60
	s_add_i32 s22, s22, s12
	s_lshl_b32 s22, s22, 6
	s_and_b32 s22, s22, 0x3f00
	s_or_b32 s22, s22, s13
	s_lshl_b32 s23, s21, 23
	s_lshl_b32 s22, s22, 9
	s_and_b32 s23, s23, 0x7000000
	s_or_b32 s22, s22, s23
	s_lshl_b32 s23, s21, 8
	s_and_b32 s23, s23, 0x100
	s_or_b32 s22, s22, s23
	s_or_b32 s23, s22, 0x4000
	s_waitcnt lgkmcnt(11)
	buffer_load_dwordx4 v[10:13], v1, s[4:7], s22 offen sc0 nt
	buffer_load_dwordx4 v[18:21], v1, s[4:7], s23 offen sc0 nt
	s_or_b32 s23, s22, 0x8000
	buffer_load_dwordx4 v[22:25], v1, s[4:7], s23 offen sc0 nt
	s_or_b32 s23, s22, 0xc000
	buffer_load_dwordx4 v[30:33], v1, s[4:7], s23 offen sc0 nt
	s_or_b32 s23, s22, 0x10000
	buffer_load_dwordx4 v[34:37], v1, s[4:7], s23 offen sc0 nt
	s_or_b32 s23, s22, 0x14000
	buffer_load_dwordx4 v[38:41], v1, s[4:7], s23 offen sc0 nt
	s_or_b32 s23, s22, 0x18000
	s_or_b32 s22, s22, 0x1c000
	buffer_load_dwordx4 v[42:45], v1, s[4:7], s23 offen sc0 nt
	buffer_load_dwordx4 v[46:49], v1, s[4:7], s22 offen sc0 nt
	v_mfma_f32_16x16x32_bf16 v[174:177], v[178:181], v[206:209], v[240:243]
	v_mfma_f32_16x16x32_bf16 v[170:173], v[194:197], v[206:209], v[244:247]
	v_mfma_f32_16x16x32_bf16 v[158:161], v[198:201], v[206:209], v[248:251]
	v_mfma_f32_16x16x32_bf16 v[142:145], v[202:205], v[206:209], v[252:255]
	s_waitcnt lgkmcnt(10)
	v_mfma_f32_16x16x32_bf16 v[166:169], v[178:181], v[210:213], v[240:243]
	v_mfma_f32_16x16x32_bf16 v[162:165], v[194:197], v[210:213], v[244:247]
	v_mfma_f32_16x16x32_bf16 v[146:149], v[198:201], v[210:213], v[248:251]
	v_mfma_f32_16x16x32_bf16 v[122:125], v[202:205], v[210:213], v[252:255]
	s_waitcnt lgkmcnt(9)
	v_mfma_f32_16x16x32_bf16 v[154:157], v[178:181], v[214:217], v[240:243]
	v_mfma_f32_16x16x32_bf16 v[150:153], v[194:197], v[214:217], v[244:247]
	v_mfma_f32_16x16x32_bf16 v[130:133], v[198:201], v[214:217], v[248:251]
	v_mfma_f32_16x16x32_bf16 v[106:109], v[202:205], v[214:217], v[252:255]
	s_waitcnt lgkmcnt(8)
	v_mfma_f32_16x16x32_bf16 v[138:141], v[178:181], v[218:221], v[240:243]
	v_mfma_f32_16x16x32_bf16 v[134:137], v[194:197], v[218:221], v[244:247]
	v_mfma_f32_16x16x32_bf16 v[114:117], v[198:201], v[218:221], v[248:251]
	v_mfma_f32_16x16x32_bf16 v[90:93], v[202:205], v[218:221], v[252:255]
	s_waitcnt lgkmcnt(7)
	v_mfma_f32_16x16x32_bf16 v[126:129], v[178:181], v[222:225], v[240:243]
	v_mfma_f32_16x16x32_bf16 v[118:121], v[194:197], v[222:225], v[244:247]
	v_mfma_f32_16x16x32_bf16 v[98:101], v[198:201], v[222:225], v[248:251]
	v_mfma_f32_16x16x32_bf16 v[74:77], v[202:205], v[222:225], v[252:255]
	s_waitcnt lgkmcnt(6)
	v_mfma_f32_16x16x32_bf16 v[110:113], v[178:181], v[226:229], v[240:243]
	v_mfma_f32_16x16x32_bf16 v[102:105], v[194:197], v[226:229], v[244:247]
	v_mfma_f32_16x16x32_bf16 v[82:85], v[198:201], v[226:229], v[248:251]
	v_mfma_f32_16x16x32_bf16 v[62:65], v[202:205], v[226:229], v[252:255]
	s_waitcnt lgkmcnt(5)
	v_mfma_f32_16x16x32_bf16 v[94:97], v[178:181], v[230:233], v[240:243]
	v_mfma_f32_16x16x32_bf16 v[86:89], v[194:197], v[230:233], v[244:247]
	v_mfma_f32_16x16x32_bf16 v[70:73], v[198:201], v[230:233], v[248:251]
	v_mfma_f32_16x16x32_bf16 v[54:57], v[202:205], v[230:233], v[252:255]
	s_waitcnt lgkmcnt(4)
	v_mfma_f32_16x16x32_bf16 v[78:81], v[178:181], v[234:237], v[240:243]
	v_mfma_f32_16x16x32_bf16 v[66:69], v[194:197], v[234:237], v[244:247]
	v_mfma_f32_16x16x32_bf16 v[58:61], v[198:201], v[234:237], v[248:251]
	v_mfma_f32_16x16x32_bf16 v[50:53], v[202:205], v[234:237], v[252:255]
	s_setprio 0
	s_waitcnt lgkmcnt(0)
	s_barrier
	ds_read_b128 v[178:181], v182 offset:33792
	ds_read_b128 v[194:197], v182 offset:35840
	ds_read_b128 v[198:201], v182 offset:37888
	ds_read_b128 v[202:205], v182 offset:39936
	ds_read_b128 v[206:209], v238 offset:1024
	ds_read_b128 v[210:213], v238 offset:3072
	ds_read_b128 v[214:217], v238 offset:5120
	ds_read_b128 v[218:221], v238 offset:7168
	ds_read_b128 v[222:225], v238 offset:9216
	ds_read_b128 v[226:229], v238 offset:11264
	ds_read_b128 v[230:233], v238 offset:13312
	ds_read_b128 v[234:237], v238 offset:15360
	v_add_u32_e32 v182, s19, v190
	s_waitcnt vmcnt(43)
	ds_write_b128 v182, v[2:5] offset:32768
	s_waitcnt vmcnt(42)
	ds_write_b128 v182, v[6:9] offset:40960
	s_waitcnt vmcnt(41)
	ds_write_b128 v182, v[14:17] offset:49152
	s_waitcnt vmcnt(40)
	ds_write_b128 v182, v[26:29] offset:57344
	s_waitcnt lgkmcnt(0)
	s_barrier
	s_setprio 1
	s_lshl_b32 s21, s21, 7
	s_and_b32 s21, s21, 0x780
	s_or_b32 s21, s21, s14
	s_or_b32 s22, s21, 0x20000
	s_waitcnt lgkmcnt(11)
	v_mfma_f32_16x16x32_bf16 v[174:177], v[178:181], v[206:209], v[174:177]
	v_mfma_f32_16x16x32_bf16 v[170:173], v[194:197], v[206:209], v[170:173]
	v_mfma_f32_16x16x32_bf16 v[158:161], v[198:201], v[206:209], v[158:161]
	v_mfma_f32_16x16x32_bf16 v[142:145], v[202:205], v[206:209], v[142:145]
	s_waitcnt lgkmcnt(10)
	v_mfma_f32_16x16x32_bf16 v[166:169], v[178:181], v[210:213], v[166:169]
	v_mfma_f32_16x16x32_bf16 v[162:165], v[194:197], v[210:213], v[162:165]
	buffer_load_dwordx4 v[2:5], v188, s[0:3], s21 offen sc1
	v_mfma_f32_16x16x32_bf16 v[146:149], v[198:201], v[210:213], v[146:149]
	v_mfma_f32_16x16x32_bf16 v[122:125], v[202:205], v[210:213], v[122:125]
	s_waitcnt lgkmcnt(9)
	v_mfma_f32_16x16x32_bf16 v[154:157], v[178:181], v[214:217], v[154:157]
	v_mfma_f32_16x16x32_bf16 v[150:153], v[194:197], v[214:217], v[150:153]
	v_mfma_f32_16x16x32_bf16 v[130:133], v[198:201], v[214:217], v[130:133]
	v_mfma_f32_16x16x32_bf16 v[106:109], v[202:205], v[214:217], v[106:109]
	s_waitcnt lgkmcnt(8)
	v_mfma_f32_16x16x32_bf16 v[138:141], v[178:181], v[218:221], v[138:141]
	v_mfma_f32_16x16x32_bf16 v[134:137], v[194:197], v[218:221], v[134:137]
	buffer_load_dwordx4 v[6:9], v188, s[0:3], s22 offen sc1
	s_or_b32 s22, s21, 0x40000
	s_or_b32 s21, s21, 0x60000
	v_mfma_f32_16x16x32_bf16 v[114:117], v[198:201], v[218:221], v[114:117]
	v_mfma_f32_16x16x32_bf16 v[90:93], v[202:205], v[218:221], v[90:93]
	s_waitcnt lgkmcnt(7)
	v_mfma_f32_16x16x32_bf16 v[126:129], v[178:181], v[222:225], v[126:129]
	v_mfma_f32_16x16x32_bf16 v[118:121], v[194:197], v[222:225], v[118:121]
	v_mfma_f32_16x16x32_bf16 v[98:101], v[198:201], v[222:225], v[98:101]
	v_mfma_f32_16x16x32_bf16 v[74:77], v[202:205], v[222:225], v[74:77]
	s_waitcnt lgkmcnt(6)
	v_mfma_f32_16x16x32_bf16 v[110:113], v[178:181], v[226:229], v[110:113]
	v_mfma_f32_16x16x32_bf16 v[102:105], v[194:197], v[226:229], v[102:105]
	buffer_load_dwordx4 v[14:17], v188, s[0:3], s22 offen sc1
	v_mfma_f32_16x16x32_bf16 v[82:85], v[198:201], v[226:229], v[82:85]
	v_mfma_f32_16x16x32_bf16 v[62:65], v[202:205], v[226:229], v[62:65]
	s_waitcnt lgkmcnt(5)
	v_mfma_f32_16x16x32_bf16 v[94:97], v[178:181], v[230:233], v[94:97]
	v_mfma_f32_16x16x32_bf16 v[86:89], v[194:197], v[230:233], v[86:89]
	v_mfma_f32_16x16x32_bf16 v[70:73], v[198:201], v[230:233], v[70:73]
	v_mfma_f32_16x16x32_bf16 v[54:57], v[202:205], v[230:233], v[54:57]
	s_waitcnt lgkmcnt(4)
	v_mfma_f32_16x16x32_bf16 v[78:81], v[178:181], v[234:237], v[78:81]
	v_mfma_f32_16x16x32_bf16 v[66:69], v[194:197], v[234:237], v[66:69]
	buffer_load_dwordx4 v[26:29], v188, s[0:3], s21 offen sc1
	v_mfma_f32_16x16x32_bf16 v[58:61], v[198:201], v[234:237], v[58:61]
	v_mfma_f32_16x16x32_bf16 v[50:53], v[202:205], v[234:237], v[50:53]
	s_setprio 0
	s_branch .LBB1_3
.Lt30:
	v_add_u32_e32 v182, s19, v191
	v_add_u32_e32 v238, s19, v192
	ds_read_b128 v[178:181], v182 offset:32768
	ds_read_b128 v[194:197], v182 offset:34816
	ds_read_b128 v[198:201], v182 offset:36864
	ds_read_b128 v[202:205], v182 offset:38912
	ds_read_b128 v[206:209], v238
	ds_read_b128 v[210:213], v238 offset:2048
	ds_read_b128 v[214:217], v238 offset:4096
	ds_read_b128 v[218:221], v238 offset:6144
	ds_read_b128 v[222:225], v238 offset:8192
	ds_read_b128 v[226:229], v238 offset:10240
	ds_read_b128 v[230:233], v238 offset:12288
	ds_read_b128 v[234:237], v238 offset:14336
	s_min_u32 s21, s20, 29
	s_xor_b32 s19, s19, 0x10000
	v_add_u32_e32 v239, s19, v189
	s_waitcnt vmcnt(11)
	v_cvt_pk_bf16_f32 v13, v12, v13
	v_cvt_pk_bf16_f32 v12, v10, v11
	s_waitcnt vmcnt(10)
	v_cvt_pk_bf16_f32 v11, v20, v21
	v_cvt_pk_bf16_f32 v10, v18, v19
	ds_write2st64_b64 v239, v[12:13], v[10:11] offset1:8
	s_waitcnt vmcnt(9)
	v_cvt_pk_bf16_f32 v11, v24, v25
	v_cvt_pk_bf16_f32 v10, v22, v23
	s_waitcnt vmcnt(8)
	v_cvt_pk_bf16_f32 v13, v32, v33
	v_cvt_pk_bf16_f32 v12, v30, v31
	ds_write2st64_b64 v239, v[10:11], v[12:13] offset0:16 offset1:24
	s_waitcnt vmcnt(7)
	v_cvt_pk_bf16_f32 v11, v36, v37
	v_cvt_pk_bf16_f32 v10, v34, v35
	s_waitcnt vmcnt(6)
	v_cvt_pk_bf16_f32 v13, v40, v41
	v_cvt_pk_bf16_f32 v12, v38, v39
	ds_write2st64_b64 v239, v[10:11], v[12:13] offset0:32 offset1:40
	s_waitcnt vmcnt(5)
	v_cvt_pk_bf16_f32 v11, v44, v45
	v_cvt_pk_bf16_f32 v10, v42, v43
	s_waitcnt vmcnt(4)
	v_cvt_pk_bf16_f32 v13, v48, v49
	v_cvt_pk_bf16_f32 v12, v46, v47
	ds_write2st64_b64 v239, v[10:11], v[12:13] offset0:48 offset1:56
	s_waitcnt lgkmcnt(0)
	s_add_i32 s21, s21, 2
	s_barrier
	s_setprio 1
	s_lshl_b32 s22, s21, 1
	s_and_b32 s22, s22, 0x60
	s_add_i32 s22, s22, s12
	s_lshl_b32 s22, s22, 6
	s_and_b32 s22, s22, 0x3f00
	s_or_b32 s22, s22, s13
	s_lshl_b32 s23, s21, 23
	s_lshl_b32 s22, s22, 9
	s_and_b32 s23, s23, 0x7000000
	s_or_b32 s22, s22, s23
	s_lshl_b32 s23, s21, 8
	s_and_b32 s23, s23, 0x100
	s_or_b32 s22, s22, s23
	s_or_b32 s23, s22, 0x4000
	s_waitcnt lgkmcnt(11)
	s_or_b32 s23, s22, 0x8000
	s_or_b32 s23, s22, 0xc000
	s_or_b32 s23, s22, 0x10000
	s_or_b32 s23, s22, 0x14000
	s_or_b32 s23, s22, 0x18000
	s_or_b32 s22, s22, 0x1c000
	v_mfma_f32_16x16x32_bf16 v[174:177], v[178:181], v[206:209], v[174:177]
	v_mfma_f32_16x16x32_bf16 v[170:173], v[194:197], v[206:209], v[170:173]
	v_mfma_f32_16x16x32_bf16 v[158:161], v[198:201], v[206:209], v[158:161]
	v_mfma_f32_16x16x32_bf16 v[142:145], v[202:205], v[206:209], v[142:145]
	s_waitcnt lgkmcnt(10)
	v_mfma_f32_16x16x32_bf16 v[166:169], v[178:181], v[210:213], v[166:169]
	v_mfma_f32_16x16x32_bf16 v[162:165], v[194:197], v[210:213], v[162:165]
	v_mfma_f32_16x16x32_bf16 v[146:149], v[198:201], v[210:213], v[146:149]
	v_mfma_f32_16x16x32_bf16 v[122:125], v[202:205], v[210:213], v[122:125]
	s_waitcnt lgkmcnt(9)
	v_mfma_f32_16x16x32_bf16 v[154:157], v[178:181], v[214:217], v[154:157]
	v_mfma_f32_16x16x32_bf16 v[150:153], v[194:197], v[214:217], v[150:153]
	v_mfma_f32_16x16x32_bf16 v[130:133], v[198:201], v[214:217], v[130:133]
	v_mfma_f32_16x16x32_bf16 v[106:109], v[202:205], v[214:217], v[106:109]
	s_waitcnt lgkmcnt(8)
	v_mfma_f32_16x16x32_bf16 v[138:141], v[178:181], v[218:221], v[138:141]
	v_mfma_f32_16x16x32_bf16 v[134:137], v[194:197], v[218:221], v[134:137]
	v_mfma_f32_16x16x32_bf16 v[114:117], v[198:201], v[218:221], v[114:117]
	v_mfma_f32_16x16x32_bf16 v[90:93], v[202:205], v[218:221], v[90:93]
	s_waitcnt lgkmcnt(7)
	v_mfma_f32_16x16x32_bf16 v[126:129], v[178:181], v[222:225], v[126:129]
	v_mfma_f32_16x16x32_bf16 v[118:121], v[194:197], v[222:225], v[118:121]
	v_mfma_f32_16x16x32_bf16 v[98:101], v[198:201], v[222:225], v[98:101]
	v_mfma_f32_16x16x32_bf16 v[74:77], v[202:205], v[222:225], v[74:77]
	s_waitcnt lgkmcnt(6)
	v_mfma_f32_16x16x32_bf16 v[110:113], v[178:181], v[226:229], v[110:113]
	v_mfma_f32_16x16x32_bf16 v[102:105], v[194:197], v[226:229], v[102:105]
	v_mfma_f32_16x16x32_bf16 v[82:85], v[198:201], v[226:229], v[82:85]
	v_mfma_f32_16x16x32_bf16 v[62:65], v[202:205], v[226:229], v[62:65]
	s_waitcnt lgkmcnt(5)
	v_mfma_f32_16x16x32_bf16 v[94:97], v[178:181], v[230:233], v[94:97]
	v_mfma_f32_16x16x32_bf16 v[86:89], v[194:197], v[230:233], v[86:89]
	v_mfma_f32_16x16x32_bf16 v[70:73], v[198:201], v[230:233], v[70:73]
	v_mfma_f32_16x16x32_bf16 v[54:57], v[202:205], v[230:233], v[54:57]
	s_waitcnt lgkmcnt(4)
	v_mfma_f32_16x16x32_bf16 v[78:81], v[178:181], v[234:237], v[78:81]
	v_mfma_f32_16x16x32_bf16 v[66:69], v[194:197], v[234:237], v[66:69]
	v_mfma_f32_16x16x32_bf16 v[58:61], v[198:201], v[234:237], v[58:61]
	v_mfma_f32_16x16x32_bf16 v[50:53], v[202:205], v[234:237], v[50:53]
	s_setprio 0
	s_waitcnt lgkmcnt(0)
	s_barrier
	ds_read_b128 v[178:181], v182 offset:33792
	ds_read_b128 v[194:197], v182 offset:35840
	ds_read_b128 v[198:201], v182 offset:37888
	ds_read_b128 v[202:205], v182 offset:39936
	ds_read_b128 v[206:209], v238 offset:1024
	ds_read_b128 v[210:213], v238 offset:3072
	ds_read_b128 v[214:217], v238 offset:5120
	ds_read_b128 v[218:221], v238 offset:7168
	ds_read_b128 v[222:225], v238 offset:9216
	ds_read_b128 v[226:229], v238 offset:11264
	ds_read_b128 v[230:233], v238 offset:13312
	ds_read_b128 v[234:237], v238 offset:15360
	v_add_u32_e32 v182, s19, v190
	s_waitcnt vmcnt(3)
	ds_write_b128 v182, v[2:5] offset:32768
	s_waitcnt vmcnt(2)
	ds_write_b128 v182, v[6:9] offset:40960
	s_waitcnt vmcnt(1)
	ds_write_b128 v182, v[14:17] offset:49152
	s_waitcnt vmcnt(0)
	ds_write_b128 v182, v[26:29] offset:57344
	s_waitcnt lgkmcnt(0)
	s_barrier
	s_setprio 1
	s_lshl_b32 s21, s21, 7
	s_and_b32 s21, s21, 0x780
	s_or_b32 s21, s21, s14
	s_or_b32 s22, s21, 0x20000
	s_waitcnt lgkmcnt(11)
	v_mfma_f32_16x16x32_bf16 v[174:177], v[178:181], v[206:209], v[174:177]
	v_mfma_f32_16x16x32_bf16 v[170:173], v[194:197], v[206:209], v[170:173]
	v_mfma_f32_16x16x32_bf16 v[158:161], v[198:201], v[206:209], v[158:161]
	v_mfma_f32_16x16x32_bf16 v[142:145], v[202:205], v[206:209], v[142:145]
	s_waitcnt lgkmcnt(10)
	v_mfma_f32_16x16x32_bf16 v[166:169], v[178:181], v[210:213], v[166:169]
	v_mfma_f32_16x16x32_bf16 v[162:165], v[194:197], v[210:213], v[162:165]
	v_mfma_f32_16x16x32_bf16 v[146:149], v[198:201], v[210:213], v[146:149]
	v_mfma_f32_16x16x32_bf16 v[122:125], v[202:205], v[210:213], v[122:125]
	s_waitcnt lgkmcnt(9)
	v_mfma_f32_16x16x32_bf16 v[154:157], v[178:181], v[214:217], v[154:157]
	v_mfma_f32_16x16x32_bf16 v[150:153], v[194:197], v[214:217], v[150:153]
	v_mfma_f32_16x16x32_bf16 v[130:133], v[198:201], v[214:217], v[130:133]
	v_mfma_f32_16x16x32_bf16 v[106:109], v[202:205], v[214:217], v[106:109]
	s_waitcnt lgkmcnt(8)
	v_mfma_f32_16x16x32_bf16 v[138:141], v[178:181], v[218:221], v[138:141]
	v_mfma_f32_16x16x32_bf16 v[134:137], v[194:197], v[218:221], v[134:137]
	s_or_b32 s22, s21, 0x40000
	s_or_b32 s21, s21, 0x60000
	v_mfma_f32_16x16x32_bf16 v[114:117], v[198:201], v[218:221], v[114:117]
	v_mfma_f32_16x16x32_bf16 v[90:93], v[202:205], v[218:221], v[90:93]
	s_waitcnt lgkmcnt(7)
	v_mfma_f32_16x16x32_bf16 v[126:129], v[178:181], v[222:225], v[126:129]
	v_mfma_f32_16x16x32_bf16 v[118:121], v[194:197], v[222:225], v[118:121]
	v_mfma_f32_16x16x32_bf16 v[98:101], v[198:201], v[222:225], v[98:101]
	v_mfma_f32_16x16x32_bf16 v[74:77], v[202:205], v[222:225], v[74:77]
	s_waitcnt lgkmcnt(6)
	v_mfma_f32_16x16x32_bf16 v[110:113], v[178:181], v[226:229], v[110:113]
	v_mfma_f32_16x16x32_bf16 v[102:105], v[194:197], v[226:229], v[102:105]
	v_mfma_f32_16x16x32_bf16 v[82:85], v[198:201], v[226:229], v[82:85]
	v_mfma_f32_16x16x32_bf16 v[62:65], v[202:205], v[226:229], v[62:65]
	s_waitcnt lgkmcnt(5)
	v_mfma_f32_16x16x32_bf16 v[94:97], v[178:181], v[230:233], v[94:97]
	v_mfma_f32_16x16x32_bf16 v[86:89], v[194:197], v[230:233], v[86:89]
	v_mfma_f32_16x16x32_bf16 v[70:73], v[198:201], v[230:233], v[70:73]
	v_mfma_f32_16x16x32_bf16 v[54:57], v[202:205], v[230:233], v[54:57]
	s_waitcnt lgkmcnt(4)
	v_mfma_f32_16x16x32_bf16 v[78:81], v[178:181], v[234:237], v[78:81]
	v_mfma_f32_16x16x32_bf16 v[66:69], v[194:197], v[234:237], v[66:69]
	v_mfma_f32_16x16x32_bf16 v[58:61], v[198:201], v[234:237], v[58:61]
	v_mfma_f32_16x16x32_bf16 v[50:53], v[202:205], v[234:237], v[50:53]
	s_setprio 0
	s_waitcnt lgkmcnt(0)
	s_barrier
	s_add_i32 s20, s20, 1
	s_add_i32 s18, s18, 2
	v_add_u32_e32 v182, s19, v191
	v_add_u32_e32 v238, s19, v192
	ds_read_b128 v[178:181], v182 offset:32768
	ds_read_b128 v[194:197], v182 offset:34816
	ds_read_b128 v[198:201], v182 offset:36864
	ds_read_b128 v[202:205], v182 offset:38912
	ds_read_b128 v[206:209], v238
	ds_read_b128 v[210:213], v238 offset:2048
	ds_read_b128 v[214:217], v238 offset:4096
	ds_read_b128 v[218:221], v238 offset:6144
	ds_read_b128 v[222:225], v238 offset:8192
	ds_read_b128 v[226:229], v238 offset:10240
	ds_read_b128 v[230:233], v238 offset:12288
	ds_read_b128 v[234:237], v238 offset:14336
	s_min_u32 s21, s20, 29
	s_xor_b32 s19, s19, 0x10000
	v_add_u32_e32 v239, s19, v189
	s_waitcnt lgkmcnt(0)
	s_add_i32 s21, s21, 2
	s_barrier
	s_setprio 1
	s_lshl_b32 s22, s21, 1
	s_and_b32 s22, s22, 0x60
	s_add_i32 s22, s22, s12
	s_lshl_b32 s22, s22, 6
	s_and_b32 s22, s22, 0x3f00
	s_or_b32 s22, s22, s13
	s_lshl_b32 s23, s21, 23
	s_lshl_b32 s22, s22, 9
	s_and_b32 s23, s23, 0x7000000
	s_or_b32 s22, s22, s23
	s_lshl_b32 s23, s21, 8
	s_and_b32 s23, s23, 0x100
	s_or_b32 s22, s22, s23
	s_or_b32 s23, s22, 0x4000
	s_waitcnt lgkmcnt(11)
	s_or_b32 s23, s22, 0x8000
	s_or_b32 s23, s22, 0xc000
	s_or_b32 s23, s22, 0x10000
	s_or_b32 s23, s22, 0x14000
	s_or_b32 s23, s22, 0x18000
	s_or_b32 s22, s22, 0x1c000
	v_mfma_f32_16x16x32_bf16 v[174:177], v[178:181], v[206:209], v[174:177]
	v_mfma_f32_16x16x32_bf16 v[170:173], v[194:197], v[206:209], v[170:173]
	v_mfma_f32_16x16x32_bf16 v[158:161], v[198:201], v[206:209], v[158:161]
	v_mfma_f32_16x16x32_bf16 v[142:145], v[202:205], v[206:209], v[142:145]
	s_waitcnt lgkmcnt(10)
	v_mfma_f32_16x16x32_bf16 v[166:169], v[178:181], v[210:213], v[166:169]
	v_mfma_f32_16x16x32_bf16 v[162:165], v[194:197], v[210:213], v[162:165]
	v_mfma_f32_16x16x32_bf16 v[146:149], v[198:201], v[210:213], v[146:149]
	v_mfma_f32_16x16x32_bf16 v[122:125], v[202:205], v[210:213], v[122:125]
	s_waitcnt lgkmcnt(9)
	v_mfma_f32_16x16x32_bf16 v[154:157], v[178:181], v[214:217], v[154:157]
	v_mfma_f32_16x16x32_bf16 v[150:153], v[194:197], v[214:217], v[150:153]
	v_mfma_f32_16x16x32_bf16 v[130:133], v[198:201], v[214:217], v[130:133]
	v_mfma_f32_16x16x32_bf16 v[106:109], v[202:205], v[214:217], v[106:109]
	s_waitcnt lgkmcnt(8)
	v_mfma_f32_16x16x32_bf16 v[138:141], v[178:181], v[218:221], v[138:141]
	v_mfma_f32_16x16x32_bf16 v[134:137], v[194:197], v[218:221], v[134:137]
	v_mfma_f32_16x16x32_bf16 v[114:117], v[198:201], v[218:221], v[114:117]
	v_mfma_f32_16x16x32_bf16 v[90:93], v[202:205], v[218:221], v[90:93]
	s_waitcnt lgkmcnt(7)
	v_mfma_f32_16x16x32_bf16 v[126:129], v[178:181], v[222:225], v[126:129]
	v_mfma_f32_16x16x32_bf16 v[118:121], v[194:197], v[222:225], v[118:121]
	v_mfma_f32_16x16x32_bf16 v[98:101], v[198:201], v[222:225], v[98:101]
	v_mfma_f32_16x16x32_bf16 v[74:77], v[202:205], v[222:225], v[74:77]
	s_waitcnt lgkmcnt(6)
	v_mfma_f32_16x16x32_bf16 v[110:113], v[178:181], v[226:229], v[110:113]
	v_mfma_f32_16x16x32_bf16 v[102:105], v[194:197], v[226:229], v[102:105]
	v_mfma_f32_16x16x32_bf16 v[82:85], v[198:201], v[226:229], v[82:85]
	v_mfma_f32_16x16x32_bf16 v[62:65], v[202:205], v[226:229], v[62:65]
	s_waitcnt lgkmcnt(5)
	v_mfma_f32_16x16x32_bf16 v[94:97], v[178:181], v[230:233], v[94:97]
	v_mfma_f32_16x16x32_bf16 v[86:89], v[194:197], v[230:233], v[86:89]
	v_mfma_f32_16x16x32_bf16 v[70:73], v[198:201], v[230:233], v[70:73]
	v_mfma_f32_16x16x32_bf16 v[54:57], v[202:205], v[230:233], v[54:57]
	s_waitcnt lgkmcnt(4)
	v_mfma_f32_16x16x32_bf16 v[78:81], v[178:181], v[234:237], v[78:81]
	v_mfma_f32_16x16x32_bf16 v[66:69], v[194:197], v[234:237], v[66:69]
	v_mfma_f32_16x16x32_bf16 v[58:61], v[198:201], v[234:237], v[58:61]
	v_mfma_f32_16x16x32_bf16 v[50:53], v[202:205], v[234:237], v[50:53]
	s_setprio 0
	s_waitcnt lgkmcnt(0)
	s_barrier
	ds_read_b128 v[178:181], v182 offset:33792
	ds_read_b128 v[194:197], v182 offset:35840
	ds_read_b128 v[198:201], v182 offset:37888
	ds_read_b128 v[202:205], v182 offset:39936
	ds_read_b128 v[206:209], v238 offset:1024
	ds_read_b128 v[210:213], v238 offset:3072
	ds_read_b128 v[214:217], v238 offset:5120
	ds_read_b128 v[218:221], v238 offset:7168
	ds_read_b128 v[222:225], v238 offset:9216
	ds_read_b128 v[226:229], v238 offset:11264
	ds_read_b128 v[230:233], v238 offset:13312
	ds_read_b128 v[234:237], v238 offset:15360
	s_waitcnt lgkmcnt(0)
	s_barrier
	s_setprio 1
	s_lshl_b32 s21, s21, 7
	s_and_b32 s21, s21, 0x780
	s_or_b32 s21, s21, s14
	s_or_b32 s22, s21, 0x20000
	s_waitcnt lgkmcnt(11)
	v_mfma_f32_16x16x32_bf16 v[174:177], v[178:181], v[206:209], v[174:177]
	v_mfma_f32_16x16x32_bf16 v[170:173], v[194:197], v[206:209], v[170:173]
	v_mfma_f32_16x16x32_bf16 v[158:161], v[198:201], v[206:209], v[158:161]
	v_mfma_f32_16x16x32_bf16 v[142:145], v[202:205], v[206:209], v[142:145]
	s_waitcnt lgkmcnt(10)
	v_mfma_f32_16x16x32_bf16 v[166:169], v[178:181], v[210:213], v[166:169]
	v_mfma_f32_16x16x32_bf16 v[162:165], v[194:197], v[210:213], v[162:165]
	v_mfma_f32_16x16x32_bf16 v[146:149], v[198:201], v[210:213], v[146:149]
	v_mfma_f32_16x16x32_bf16 v[122:125], v[202:205], v[210:213], v[122:125]
	s_waitcnt lgkmcnt(9)
	v_mfma_f32_16x16x32_bf16 v[154:157], v[178:181], v[214:217], v[154:157]
	v_mfma_f32_16x16x32_bf16 v[150:153], v[194:197], v[214:217], v[150:153]
	v_mfma_f32_16x16x32_bf16 v[130:133], v[198:201], v[214:217], v[130:133]
	v_mfma_f32_16x16x32_bf16 v[106:109], v[202:205], v[214:217], v[106:109]
	s_waitcnt lgkmcnt(8)
	v_mfma_f32_16x16x32_bf16 v[138:141], v[178:181], v[218:221], v[138:141]
	v_mfma_f32_16x16x32_bf16 v[134:137], v[194:197], v[218:221], v[134:137]
	s_or_b32 s22, s21, 0x40000
	s_or_b32 s21, s21, 0x60000
	v_mfma_f32_16x16x32_bf16 v[114:117], v[198:201], v[218:221], v[114:117]
	v_mfma_f32_16x16x32_bf16 v[90:93], v[202:205], v[218:221], v[90:93]
	s_waitcnt lgkmcnt(7)
	v_mfma_f32_16x16x32_bf16 v[126:129], v[178:181], v[222:225], v[126:129]
	v_mfma_f32_16x16x32_bf16 v[118:121], v[194:197], v[222:225], v[118:121]
	v_mfma_f32_16x16x32_bf16 v[98:101], v[198:201], v[222:225], v[98:101]
	v_mfma_f32_16x16x32_bf16 v[74:77], v[202:205], v[222:225], v[74:77]
	s_waitcnt lgkmcnt(6)
	v_mfma_f32_16x16x32_bf16 v[110:113], v[178:181], v[226:229], v[110:113]
	v_mfma_f32_16x16x32_bf16 v[102:105], v[194:197], v[226:229], v[102:105]
	v_mfma_f32_16x16x32_bf16 v[82:85], v[198:201], v[226:229], v[82:85]
	v_mfma_f32_16x16x32_bf16 v[62:65], v[202:205], v[226:229], v[62:65]
	s_waitcnt lgkmcnt(5)
	v_mfma_f32_16x16x32_bf16 v[94:97], v[178:181], v[230:233], v[94:97]
	v_mfma_f32_16x16x32_bf16 v[86:89], v[194:197], v[230:233], v[86:89]
	v_mfma_f32_16x16x32_bf16 v[70:73], v[198:201], v[230:233], v[70:73]
	v_mfma_f32_16x16x32_bf16 v[54:57], v[202:205], v[230:233], v[54:57]
	s_waitcnt lgkmcnt(4)
	v_mfma_f32_16x16x32_bf16 v[78:81], v[178:181], v[234:237], v[78:81]
	v_mfma_f32_16x16x32_bf16 v[66:69], v[194:197], v[234:237], v[66:69]
	v_mfma_f32_16x16x32_bf16 v[58:61], v[198:201], v[234:237], v[58:61]
	v_mfma_f32_16x16x32_bf16 v[50:53], v[202:205], v[234:237], v[50:53]
	s_setprio 0
	s_and_b32 s21, s18, 32
	s_add_i32 s21, s21, s12
	s_lshl_b32 s21, s21, 6
	s_and_b32 s21, s21, 0x3f00
	v_add_lshl_u32 v182, v193, s21, 9
	v_lshl_add_u64 v[206:207], v[184:185], 0, v[182:183]
	v_add_co_u32_e32 v208, vcc, s8, v206
	s_nop 1
	v_addc_co_u32_e32 v209, vcc, 0, v207, vcc
	v_add_co_u32_e32 v210, vcc, s15, v206
	s_nop 1
	v_addc_co_u32_e32 v211, vcc, 0, v207, vcc
	v_add_co_u32_e32 v212, vcc, s9, v206
	s_nop 1
	v_addc_co_u32_e32 v213, vcc, 0, v207, vcc
	v_add_co_u32_e32 v214, vcc, s16, v206
	s_nop 1
	v_addc_co_u32_e32 v215, vcc, 0, v207, vcc
	v_add_co_u32_e32 v216, vcc, s10, v206
	s_nop 1
	v_addc_co_u32_e32 v217, vcc, 0, v207, vcc
	v_add_co_u32_e32 v218, vcc, s17, v206
	s_nop 1
	v_addc_co_u32_e32 v219, vcc, 0, v207, vcc
	v_add_co_u32_e32 v220, vcc, s11, v206
	s_nop 1
	v_addc_co_u32_e32 v221, vcc, 0, v207, vcc
	global_store_dwordx4 v[206:207], v[174:177], off
	global_store_dwordx4 v[206:207], v[170:173], off offset:64
	global_store_dwordx4 v[206:207], v[158:161], off offset:128
	global_store_dwordx4 v[206:207], v[142:145], off offset:192
	global_store_dwordx4 v[208:209], v[166:169], off
	global_store_dwordx4 v[208:209], v[162:165], off offset:64
	global_store_dwordx4 v[208:209], v[146:149], off offset:128
	global_store_dwordx4 v[208:209], v[122:125], off offset:192
	global_store_dwordx4 v[210:211], v[154:157], off
	global_store_dwordx4 v[210:211], v[150:153], off offset:64
	global_store_dwordx4 v[210:211], v[130:133], off offset:128
	global_store_dwordx4 v[210:211], v[106:109], off offset:192
	global_store_dwordx4 v[212:213], v[138:141], off
	global_store_dwordx4 v[212:213], v[134:137], off offset:64
	global_store_dwordx4 v[212:213], v[114:117], off offset:128
	global_store_dwordx4 v[212:213], v[90:93], off offset:192
	global_store_dwordx4 v[214:215], v[126:129], off
	global_store_dwordx4 v[214:215], v[118:121], off offset:64
	global_store_dwordx4 v[214:215], v[98:101], off offset:128
	global_store_dwordx4 v[214:215], v[74:77], off offset:192
	global_store_dwordx4 v[216:217], v[110:113], off
	global_store_dwordx4 v[216:217], v[102:105], off offset:64
	global_store_dwordx4 v[216:217], v[82:85], off offset:128
	global_store_dwordx4 v[216:217], v[62:65], off offset:192
	global_store_dwordx4 v[218:219], v[94:97], off
	global_store_dwordx4 v[218:219], v[86:89], off offset:64
	global_store_dwordx4 v[218:219], v[70:73], off offset:128
	global_store_dwordx4 v[218:219], v[54:57], off offset:192
	global_store_dwordx4 v[220:221], v[78:81], off
	global_store_dwordx4 v[220:221], v[66:69], off offset:64
	global_store_dwordx4 v[220:221], v[58:61], off offset:128
	global_store_dwordx4 v[220:221], v[50:53], off offset:192
	s_waitcnt lgkmcnt(0)
	s_barrier
	s_branch .LBB1_6
.Lfirst:
	v_add_u32_e32 v182, s19, v191
	v_add_u32_e32 v238, s19, v192
	ds_read_b128 v[178:181], v182 offset:32768
	ds_read_b128 v[194:197], v182 offset:34816
	ds_read_b128 v[198:201], v182 offset:36864
	ds_read_b128 v[202:205], v182 offset:38912
	ds_read_b128 v[206:209], v238
	ds_read_b128 v[210:213], v238 offset:2048
	ds_read_b128 v[214:217], v238 offset:4096
	ds_read_b128 v[218:221], v238 offset:6144
	ds_read_b128 v[222:225], v238 offset:8192
	ds_read_b128 v[226:229], v238 offset:10240
	ds_read_b128 v[230:233], v238 offset:12288
	ds_read_b128 v[234:237], v238 offset:14336
	s_min_u32 s21, s20, 29
	s_xor_b32 s19, s19, 0x10000
	v_add_u32_e32 v239, s19, v189
	s_waitcnt vmcnt(11)
	v_cvt_pk_bf16_f32 v13, v12, v13
	v_cvt_pk_bf16_f32 v12, v10, v11
	s_waitcnt vmcnt(10)
	v_cvt_pk_bf16_f32 v11, v20, v21
	v_cvt_pk_bf16_f32 v10, v18, v19
	ds_write2st64_b64 v239, v[12:13], v[10:11] offset1:8
	s_waitcnt vmcnt(9)
	v_cvt_pk_bf16_f32 v11, v24, v25
	v_cvt_pk_bf16_f32 v10, v22, v23
	s_waitcnt vmcnt(8)
	v_cvt_pk_bf16_f32 v13, v32, v33
	v_cvt_pk_bf16_f32 v12, v30, v31
	ds_write2st64_b64 v239, v[10:11], v[12:13] offset0:16 offset1:24
	s_waitcnt vmcnt(7)
	v_cvt_pk_bf16_f32 v11, v36, v37
	v_cvt_pk_bf16_f32 v10, v34, v35
	s_waitcnt vmcnt(6)
	v_cvt_pk_bf16_f32 v13, v40, v41
	v_cvt_pk_bf16_f32 v12, v38, v39
	ds_write2st64_b64 v239, v[10:11], v[12:13] offset0:32 offset1:40
	s_waitcnt vmcnt(5)
	v_cvt_pk_bf16_f32 v11, v44, v45
	v_cvt_pk_bf16_f32 v10, v42, v43
	s_waitcnt vmcnt(4)
	v_cvt_pk_bf16_f32 v13, v48, v49
	v_cvt_pk_bf16_f32 v12, v46, v47
	ds_write2st64_b64 v239, v[10:11], v[12:13] offset0:48 offset1:56
	s_waitcnt lgkmcnt(0)
	s_add_i32 s21, s21, 2
	s_barrier
	s_setprio 1
	s_lshl_b32 s22, s21, 1
	s_and_b32 s22, s22, 0x60
	s_add_i32 s22, s22, s12
	s_lshl_b32 s22, s22, 6
	s_and_b32 s22, s22, 0x3f00
	s_or_b32 s22, s22, s13
	s_lshl_b32 s23, s21, 23
	s_lshl_b32 s22, s22, 9
	s_and_b32 s23, s23, 0x7000000
	s_or_b32 s22, s22, s23
	s_lshl_b32 s23, s21, 8
	s_and_b32 s23, s23, 0x100
	s_or_b32 s22, s22, s23
	s_or_b32 s23, s22, 0x4000
	s_waitcnt lgkmcnt(11)
	buffer_load_dwordx4 v[10:13], v1, s[4:7], s22 offen sc0 nt
	buffer_load_dwordx4 v[18:21], v1, s[4:7], s23 offen sc0 nt
	s_or_b32 s23, s22, 0x8000
	buffer_load_dwordx4 v[22:25], v1, s[4:7], s23 offen sc0 nt
	s_or_b32 s23, s22, 0xc000
	buffer_load_dwordx4 v[30:33], v1, s[4:7], s23 offen sc0 nt
	s_or_b32 s23, s22, 0x10000
	buffer_load_dwordx4 v[34:37], v1, s[4:7], s23 offen sc0 nt
	s_or_b32 s23, s22, 0x14000
	buffer_load_dwordx4 v[38:41], v1, s[4:7], s23 offen sc0 nt
	s_or_b32 s23, s22, 0x18000
	s_or_b32 s22, s22, 0x1c000
	buffer_load_dwordx4 v[42:45], v1, s[4:7], s23 offen sc0 nt
	buffer_load_dwordx4 v[46:49], v1, s[4:7], s22 offen sc0 nt
	v_mfma_f32_16x16x32_bf16 v[174:177], v[178:181], v[206:209], v[240:243]
	v_mfma_f32_16x16x32_bf16 v[170:173], v[194:197], v[206:209], v[244:247]
	v_mfma_f32_16x16x32_bf16 v[158:161], v[198:201], v[206:209], v[248:251]
	v_mfma_f32_16x16x32_bf16 v[142:145], v[202:205], v[206:209], v[252:255]
	s_waitcnt lgkmcnt(10)
	v_mfma_f32_16x16x32_bf16 v[166:169], v[178:181], v[210:213], v[240:243]
	v_mfma_f32_16x16x32_bf16 v[162:165], v[194:197], v[210:213], v[244:247]
	v_mfma_f32_16x16x32_bf16 v[146:149], v[198:201], v[210:213], v[248:251]
	v_mfma_f32_16x16x32_bf16 v[122:125], v[202:205], v[210:213], v[252:255]
	s_waitcnt lgkmcnt(9)
	v_mfma_f32_16x16x32_bf16 v[154:157], v[178:181], v[214:217], v[240:243]
	v_mfma_f32_16x16x32_bf16 v[150:153], v[194:197], v[214:217], v[244:247]
	v_mfma_f32_16x16x32_bf16 v[130:133], v[198:201], v[214:217], v[248:251]
	v_mfma_f32_16x16x32_bf16 v[106:109], v[202:205], v[214:217], v[252:255]
	s_waitcnt lgkmcnt(8)
	v_mfma_f32_16x16x32_bf16 v[138:141], v[178:181], v[218:221], v[240:243]
	v_mfma_f32_16x16x32_bf16 v[134:137], v[194:197], v[218:221], v[244:247]
	v_mfma_f32_16x16x32_bf16 v[114:117], v[198:201], v[218:221], v[248:251]
	v_mfma_f32_16x16x32_bf16 v[90:93], v[202:205], v[218:221], v[252:255]
	s_waitcnt lgkmcnt(7)
	v_mfma_f32_16x16x32_bf16 v[126:129], v[178:181], v[222:225], v[240:243]
	v_mfma_f32_16x16x32_bf16 v[118:121], v[194:197], v[222:225], v[244:247]
	v_mfma_f32_16x16x32_bf16 v[98:101], v[198:201], v[222:225], v[248:251]
	v_mfma_f32_16x16x32_bf16 v[74:77], v[202:205], v[222:225], v[252:255]
	s_waitcnt lgkmcnt(6)
	v_mfma_f32_16x16x32_bf16 v[110:113], v[178:181], v[226:229], v[240:243]
	v_mfma_f32_16x16x32_bf16 v[102:105], v[194:197], v[226:229], v[244:247]
	v_mfma_f32_16x16x32_bf16 v[82:85], v[198:201], v[226:229], v[248:251]
	v_mfma_f32_16x16x32_bf16 v[62:65], v[202:205], v[226:229], v[252:255]
	s_waitcnt lgkmcnt(5)
	v_mfma_f32_16x16x32_bf16 v[94:97], v[178:181], v[230:233], v[240:243]
	v_mfma_f32_16x16x32_bf16 v[86:89], v[194:197], v[230:233], v[244:247]
	v_mfma_f32_16x16x32_bf16 v[70:73], v[198:201], v[230:233], v[248:251]
	v_mfma_f32_16x16x32_bf16 v[54:57], v[202:205], v[230:233], v[252:255]
	s_waitcnt lgkmcnt(4)
	v_mfma_f32_16x16x32_bf16 v[78:81], v[178:181], v[234:237], v[240:243]
	v_mfma_f32_16x16x32_bf16 v[66:69], v[194:197], v[234:237], v[244:247]
	v_mfma_f32_16x16x32_bf16 v[58:61], v[198:201], v[234:237], v[248:251]
	v_mfma_f32_16x16x32_bf16 v[50:53], v[202:205], v[234:237], v[252:255]
	s_setprio 0
	s_waitcnt lgkmcnt(0)
	s_barrier
	ds_read_b128 v[178:181], v182 offset:33792
	ds_read_b128 v[194:197], v182 offset:35840
	ds_read_b128 v[198:201], v182 offset:37888
	ds_read_b128 v[202:205], v182 offset:39936
	ds_read_b128 v[206:209], v238 offset:1024
	ds_read_b128 v[210:213], v238 offset:3072
	ds_read_b128 v[214:217], v238 offset:5120
	ds_read_b128 v[218:221], v238 offset:7168
	ds_read_b128 v[222:225], v238 offset:9216
	ds_read_b128 v[226:229], v238 offset:11264
	ds_read_b128 v[230:233], v238 offset:13312
	ds_read_b128 v[234:237], v238 offset:15360
	v_add_u32_e32 v182, s19, v190
	s_waitcnt vmcnt(11)
	ds_write_b128 v182, v[2:5] offset:32768
	s_waitcnt vmcnt(10)
	ds_write_b128 v182, v[6:9] offset:40960
	s_waitcnt vmcnt(9)
	ds_write_b128 v182, v[14:17] offset:49152
	s_waitcnt vmcnt(8)
	ds_write_b128 v182, v[26:29] offset:57344
	s_waitcnt lgkmcnt(0)
	s_barrier
	s_setprio 1
	s_lshl_b32 s21, s21, 7
	s_and_b32 s21, s21, 0x780
	s_or_b32 s21, s21, s14
	s_or_b32 s22, s21, 0x20000
	s_waitcnt lgkmcnt(11)
	v_mfma_f32_16x16x32_bf16 v[174:177], v[178:181], v[206:209], v[174:177]
	v_mfma_f32_16x16x32_bf16 v[170:173], v[194:197], v[206:209], v[170:173]
	v_mfma_f32_16x16x32_bf16 v[158:161], v[198:201], v[206:209], v[158:161]
	v_mfma_f32_16x16x32_bf16 v[142:145], v[202:205], v[206:209], v[142:145]
	s_waitcnt lgkmcnt(10)
	v_mfma_f32_16x16x32_bf16 v[166:169], v[178:181], v[210:213], v[166:169]
	v_mfma_f32_16x16x32_bf16 v[162:165], v[194:197], v[210:213], v[162:165]
	buffer_load_dwordx4 v[2:5], v188, s[0:3], s21 offen sc1
	v_mfma_f32_16x16x32_bf16 v[146:149], v[198:201], v[210:213], v[146:149]
	v_mfma_f32_16x16x32_bf16 v[122:125], v[202:205], v[210:213], v[122:125]
	s_waitcnt lgkmcnt(9)
	v_mfma_f32_16x16x32_bf16 v[154:157], v[178:181], v[214:217], v[154:157]
	v_mfma_f32_16x16x32_bf16 v[150:153], v[194:197], v[214:217], v[150:153]
	v_mfma_f32_16x16x32_bf16 v[130:133], v[198:201], v[214:217], v[130:133]
	v_mfma_f32_16x16x32_bf16 v[106:109], v[202:205], v[214:217], v[106:109]
	s_waitcnt lgkmcnt(8)
	v_mfma_f32_16x16x32_bf16 v[138:141], v[178:181], v[218:221], v[138:141]
	v_mfma_f32_16x16x32_bf16 v[134:137], v[194:197], v[218:221], v[134:137]
	buffer_load_dwordx4 v[6:9], v188, s[0:3], s22 offen sc1
	s_or_b32 s22, s21, 0x40000
	s_or_b32 s21, s21, 0x60000
	v_mfma_f32_16x16x32_bf16 v[114:117], v[198:201], v[218:221], v[114:117]
	v_mfma_f32_16x16x32_bf16 v[90:93], v[202:205], v[218:221], v[90:93]
	s_waitcnt lgkmcnt(7)
	v_mfma_f32_16x16x32_bf16 v[126:129], v[178:181], v[222:225], v[126:129]
	v_mfma_f32_16x16x32_bf16 v[118:121], v[194:197], v[222:225], v[118:121]
	v_mfma_f32_16x16x32_bf16 v[98:101], v[198:201], v[222:225], v[98:101]
	v_mfma_f32_16x16x32_bf16 v[74:77], v[202:205], v[222:225], v[74:77]
	s_waitcnt lgkmcnt(6)
	v_mfma_f32_16x16x32_bf16 v[110:113], v[178:181], v[226:229], v[110:113]
	v_mfma_f32_16x16x32_bf16 v[102:105], v[194:197], v[226:229], v[102:105]
	buffer_load_dwordx4 v[14:17], v188, s[0:3], s22 offen sc1
	v_mfma_f32_16x16x32_bf16 v[82:85], v[198:201], v[226:229], v[82:85]
	v_mfma_f32_16x16x32_bf16 v[62:65], v[202:205], v[226:229], v[62:65]
	s_waitcnt lgkmcnt(5)
	v_mfma_f32_16x16x32_bf16 v[94:97], v[178:181], v[230:233], v[94:97]
	v_mfma_f32_16x16x32_bf16 v[86:89], v[194:197], v[230:233], v[86:89]
	v_mfma_f32_16x16x32_bf16 v[70:73], v[198:201], v[230:233], v[70:73]
	v_mfma_f32_16x16x32_bf16 v[54:57], v[202:205], v[230:233], v[54:57]
	s_waitcnt lgkmcnt(4)
	v_mfma_f32_16x16x32_bf16 v[78:81], v[178:181], v[234:237], v[78:81]
	v_mfma_f32_16x16x32_bf16 v[66:69], v[194:197], v[234:237], v[66:69]
	buffer_load_dwordx4 v[26:29], v188, s[0:3], s21 offen sc1
	v_mfma_f32_16x16x32_bf16 v[58:61], v[198:201], v[234:237], v[58:61]
	v_mfma_f32_16x16x32_bf16 v[50:53], v[202:205], v[234:237], v[50:53]
	s_setprio 0
	s_branch .LBB1_3
